# c1 short-conv mixer block loop rewritten: all 28 loads of an 8-row block in flight together (was one exposed latency per row), on top of flat-release barrier version
# speedup vs baseline: 1.0092x; 1.0086x over previous
.Lmix_top:
	s_add_i32 s2, s91, s9
	s_cmpk_lt_i32 s2, 0x400
	s_cselect_b32 s3, 0xf8, 56
	s_and_b32 s11, s3, s9
	s_add_i32 s0, s2, -1
	s_mul_i32 s4, s0, 0x1a00
	s_mul_hi_i32 s5, s0, 0x1a00
	s_add_u32 s4, s4, 0x1000
	s_addc_u32 s5, s5, 0
	s_add_u32 s4, s16, s4
	s_addc_u32 s5, s17, s5
	v_lshlrev_b32_e32 v68, 1, v26
	s_ashr_i32 s1, s2, 31
	s_mov_b32 s0, s2
	s_lshl_b64 s[12:13], s[0:1], 10
	v_lshl_add_u64 v[64:65], v[28:29], 0, s[12:13]
	s_mov_b64 s[0:1], 0x1000
	v_lshl_add_u64 v[210:211], v[64:65], 0, s[0:1]
	global_load_dwordx4 v[88:91], v68, s[4:5] offset:64
	global_load_dwordx4 v[128:131], v68, s[4:5] offset:1088
	s_add_u32 s4, s4, 0x1a00
	s_addc_u32 s5, s5, 0
	global_load_dwordx4 v[92:95], v68, s[4:5] offset:64
	global_load_dwordx4 v[132:135], v68, s[4:5] offset:1088
	global_load_dwordx4 v[168:171], v68, s[4:5] offset:-960
	s_add_u32 s4, s4, 0x1a00
	s_addc_u32 s5, s5, 0
	global_load_dwordx4 v[96:99], v68, s[4:5] offset:64
	global_load_dwordx4 v[136:139], v68, s[4:5] offset:1088
	global_load_dwordx4 v[172:175], v68, s[4:5] offset:-960
	s_add_u32 s4, s4, 0x1a00
	s_addc_u32 s5, s5, 0
	global_load_dwordx4 v[100:103], v68, s[4:5] offset:64
	global_load_dwordx4 v[140:143], v68, s[4:5] offset:1088
	global_load_dwordx4 v[176:179], v68, s[4:5] offset:-960
	s_add_u32 s4, s4, 0x1a00
	s_addc_u32 s5, s5, 0
	global_load_dwordx4 v[104:107], v68, s[4:5] offset:64
	global_load_dwordx4 v[144:147], v68, s[4:5] offset:1088
	global_load_dwordx4 v[180:183], v68, s[4:5] offset:-960
	s_add_u32 s4, s4, 0x1a00
	s_addc_u32 s5, s5, 0
	global_load_dwordx4 v[108:111], v68, s[4:5] offset:64
	global_load_dwordx4 v[148:151], v68, s[4:5] offset:1088
	global_load_dwordx4 v[184:187], v68, s[4:5] offset:-960
	s_add_u32 s4, s4, 0x1a00
	s_addc_u32 s5, s5, 0
	global_load_dwordx4 v[112:115], v68, s[4:5] offset:64
	global_load_dwordx4 v[152:155], v68, s[4:5] offset:1088
	global_load_dwordx4 v[188:191], v68, s[4:5] offset:-960
	s_add_u32 s4, s4, 0x1a00
	s_addc_u32 s5, s5, 0
	global_load_dwordx4 v[116:119], v68, s[4:5] offset:64
	global_load_dwordx4 v[156:159], v68, s[4:5] offset:1088
	global_load_dwordx4 v[192:195], v68, s[4:5] offset:-960
	s_add_u32 s4, s4, 0x1a00
	s_addc_u32 s5, s5, 0
	global_load_dwordx4 v[120:123], v68, s[4:5] offset:64
	global_load_dwordx4 v[160:163], v68, s[4:5] offset:1088
	global_load_dwordx4 v[200:203], v68, s[4:5] offset:-960
	s_add_u32 s4, s4, 0x1a00
	s_addc_u32 s5, s5, 0
	global_load_dwordx4 v[124:127], v68, s[4:5] offset:64
	global_load_dwordx4 v[164:167], v68, s[4:5] offset:1088
	s_waitcnt vmcnt(24)
	s_cmp_lg_u32 s11, 0
	s_cbranch_scc1 .Lmix_hasprev
	v_mov_b32_e32 v88, 0
	v_mov_b32_e32 v89, 0
	v_mov_b32_e32 v90, 0
	v_mov_b32_e32 v91, 0
	v_mov_b32_e32 v128, 0
	v_mov_b32_e32 v129, 0
	v_mov_b32_e32 v130, 0
	v_mov_b32_e32 v131, 0
.Lmix_hasprev:
	v_lshlrev_b32_e32 v18, 16, v88
	v_lshlrev_b32_e32 v70, 16, v128
	v_and_b32_e32 v19, 0xffff0000, v88
	v_and_b32_e32 v71, 0xffff0000, v128
	v_lshlrev_b32_e32 v20, 16, v89
	v_lshlrev_b32_e32 v72, 16, v129
	v_and_b32_e32 v21, 0xffff0000, v89
	v_and_b32_e32 v73, 0xffff0000, v129
	v_lshlrev_b32_e32 v22, 16, v90
	v_lshlrev_b32_e32 v74, 16, v130
	v_and_b32_e32 v23, 0xffff0000, v90
	v_and_b32_e32 v75, 0xffff0000, v130
	v_lshlrev_b32_e32 v24, 16, v91
	v_lshlrev_b32_e32 v76, 16, v131
	v_and_b32_e32 v25, 0xffff0000, v91
	v_and_b32_e32 v77, 0xffff0000, v131
	v_mul_f32_e32 v38, v18, v70
	v_mul_f32_e32 v39, v19, v71
	v_mul_f32_e32 v40, v20, v72
	v_mul_f32_e32 v41, v21, v73
	v_mul_f32_e32 v42, v22, v74
	v_mul_f32_e32 v43, v23, v75
	v_mul_f32_e32 v44, v24, v76
	v_mul_f32_e32 v45, v25, v77
	v_lshlrev_b32_e32 v18, 16, v92
	v_lshlrev_b32_e32 v70, 16, v132
	v_and_b32_e32 v19, 0xffff0000, v92
	v_and_b32_e32 v71, 0xffff0000, v132
	v_lshlrev_b32_e32 v20, 16, v93
	v_lshlrev_b32_e32 v72, 16, v133
	v_and_b32_e32 v21, 0xffff0000, v93
	v_and_b32_e32 v73, 0xffff0000, v133
	v_lshlrev_b32_e32 v22, 16, v94
	v_lshlrev_b32_e32 v74, 16, v134
	v_and_b32_e32 v23, 0xffff0000, v94
	v_and_b32_e32 v75, 0xffff0000, v134
	v_lshlrev_b32_e32 v24, 16, v95
	v_lshlrev_b32_e32 v76, 16, v135
	v_and_b32_e32 v25, 0xffff0000, v95
	v_and_b32_e32 v77, 0xffff0000, v135
	v_mul_f32_e32 v46, v18, v70
	v_mul_f32_e32 v47, v19, v71
	v_mul_f32_e32 v48, v20, v72
	v_mul_f32_e32 v49, v21, v73
	v_mul_f32_e32 v50, v22, v74
	v_mul_f32_e32 v51, v23, v75
	v_mul_f32_e32 v52, v24, v76
	v_mul_f32_e32 v53, v25, v77
	s_waitcnt vmcnt(21)
	v_lshlrev_b32_e32 v18, 16, v96
	v_lshlrev_b32_e32 v70, 16, v136
	v_and_b32_e32 v19, 0xffff0000, v96
	v_and_b32_e32 v71, 0xffff0000, v136
	v_lshlrev_b32_e32 v20, 16, v97
	v_lshlrev_b32_e32 v72, 16, v137
	v_and_b32_e32 v21, 0xffff0000, v97
	v_and_b32_e32 v73, 0xffff0000, v137
	v_lshlrev_b32_e32 v22, 16, v98
	v_lshlrev_b32_e32 v74, 16, v138
	v_and_b32_e32 v23, 0xffff0000, v98
	v_and_b32_e32 v75, 0xffff0000, v138
	v_lshlrev_b32_e32 v24, 16, v99
	v_lshlrev_b32_e32 v76, 16, v139
	v_and_b32_e32 v25, 0xffff0000, v99
	v_and_b32_e32 v77, 0xffff0000, v139
	v_mul_f32_e32 v54, v18, v70
	v_mul_f32_e32 v55, v19, v71
	v_mul_f32_e32 v56, v20, v72
	v_mul_f32_e32 v57, v21, v73
	v_mul_f32_e32 v58, v22, v74
	v_mul_f32_e32 v59, v23, v75
	v_mul_f32_e32 v60, v24, v76
	v_mul_f32_e32 v61, v25, v77
	v_lshlrev_b32_e32 v18, 16, v168
	v_and_b32_e32 v19, 0xffff0000, v168
	v_lshlrev_b32_e32 v20, 16, v169
	v_and_b32_e32 v21, 0xffff0000, v169
	v_lshlrev_b32_e32 v22, 16, v170
	v_and_b32_e32 v23, 0xffff0000, v170
	v_lshlrev_b32_e32 v24, 16, v171
	v_and_b32_e32 v25, 0xffff0000, v171
	v_mul_f32_e32 v78, v36, v38
	v_mul_f32_e32 v70, v37, v54
	v_mul_f32_e32 v79, v10, v39
	v_mul_f32_e32 v71, v11, v55
	v_mul_f32_e32 v80, v34, v40
	v_mul_f32_e32 v72, v35, v56
	v_mul_f32_e32 v81, v12, v41
	v_mul_f32_e32 v73, v13, v57
	v_mul_f32_e32 v82, v32, v42
	v_mul_f32_e32 v74, v33, v58
	v_mul_f32_e32 v83, v14, v43
	v_mul_f32_e32 v75, v15, v59
	v_mul_f32_e32 v84, v30, v44
	v_mul_f32_e32 v76, v31, v60
	v_mul_f32_e32 v85, v16, v45
	v_mul_f32_e32 v77, v17, v61
	v_fma_f32 v78, v2, v46, v78
	v_fma_f32 v79, v3, v47, v79
	v_fma_f32 v80, v4, v48, v80
	v_fma_f32 v81, v5, v49, v81
	v_fma_f32 v82, v6, v50, v82
	v_fma_f32 v83, v7, v51, v83
	v_fma_f32 v84, v8, v52, v84
	v_fma_f32 v85, v9, v53, v85
	v_add_f32_e32 v78, v78, v70
	v_add_f32_e32 v79, v79, v71
	v_add_f32_e32 v80, v80, v72
	v_add_f32_e32 v81, v81, v73
	v_add_f32_e32 v82, v82, v74
	v_add_f32_e32 v83, v83, v75
	v_add_f32_e32 v84, v84, v76
	v_add_f32_e32 v85, v85, v77
	v_mul_f32_e32 v78, v78, v18
	v_mul_f32_e32 v79, v79, v19
	v_mul_f32_e32 v80, v80, v20
	v_mul_f32_e32 v81, v81, v21
	v_mul_f32_e32 v82, v82, v22
	v_mul_f32_e32 v83, v83, v23
	v_mul_f32_e32 v84, v84, v24
	v_mul_f32_e32 v85, v85, v25
	v_cvt_pk_fp8_f32 v62, v78, v79
	v_cvt_pk_fp8_f32 v63, v82, v83
	v_cvt_pk_fp8_f32 v62, v80, v81 op_sel:[0,0,1]
	v_cvt_pk_fp8_f32 v63, v84, v85 op_sel:[0,0,1]
	global_store_dwordx2 v[64:65], v[62:63], off
	s_waitcnt vmcnt(19)
	v_lshlrev_b32_e32 v18, 16, v100
	v_lshlrev_b32_e32 v70, 16, v140
	v_and_b32_e32 v19, 0xffff0000, v100
	v_and_b32_e32 v71, 0xffff0000, v140
	v_lshlrev_b32_e32 v20, 16, v101
	v_lshlrev_b32_e32 v72, 16, v141
	v_and_b32_e32 v21, 0xffff0000, v101
	v_and_b32_e32 v73, 0xffff0000, v141
	v_lshlrev_b32_e32 v22, 16, v102
	v_lshlrev_b32_e32 v74, 16, v142
	v_and_b32_e32 v23, 0xffff0000, v102
	v_and_b32_e32 v75, 0xffff0000, v142
	v_lshlrev_b32_e32 v24, 16, v103
	v_lshlrev_b32_e32 v76, 16, v143
	v_and_b32_e32 v25, 0xffff0000, v103
	v_and_b32_e32 v77, 0xffff0000, v143
	v_mul_f32_e32 v38, v18, v70
	v_mul_f32_e32 v39, v19, v71
	v_mul_f32_e32 v40, v20, v72
	v_mul_f32_e32 v41, v21, v73
	v_mul_f32_e32 v42, v22, v74
	v_mul_f32_e32 v43, v23, v75
	v_mul_f32_e32 v44, v24, v76
	v_mul_f32_e32 v45, v25, v77
	v_lshlrev_b32_e32 v18, 16, v172
	v_and_b32_e32 v19, 0xffff0000, v172
	v_lshlrev_b32_e32 v20, 16, v173
	v_and_b32_e32 v21, 0xffff0000, v173
	v_lshlrev_b32_e32 v22, 16, v174
	v_and_b32_e32 v23, 0xffff0000, v174
	v_lshlrev_b32_e32 v24, 16, v175
	v_and_b32_e32 v25, 0xffff0000, v175
	v_mul_f32_e32 v78, v36, v46
	v_mul_f32_e32 v70, v37, v38
	v_mul_f32_e32 v79, v10, v47
	v_mul_f32_e32 v71, v11, v39
	v_mul_f32_e32 v80, v34, v48
	v_mul_f32_e32 v72, v35, v40
	v_mul_f32_e32 v81, v12, v49
	v_mul_f32_e32 v73, v13, v41
	v_mul_f32_e32 v82, v32, v50
	v_mul_f32_e32 v74, v33, v42
	v_mul_f32_e32 v83, v14, v51
	v_mul_f32_e32 v75, v15, v43
	v_mul_f32_e32 v84, v30, v52
	v_mul_f32_e32 v76, v31, v44
	v_mul_f32_e32 v85, v16, v53
	v_mul_f32_e32 v77, v17, v45
	v_fma_f32 v78, v2, v54, v78
	v_fma_f32 v79, v3, v55, v79
	v_fma_f32 v80, v4, v56, v80
	v_fma_f32 v81, v5, v57, v81
	v_fma_f32 v82, v6, v58, v82
	v_fma_f32 v83, v7, v59, v83
	v_fma_f32 v84, v8, v60, v84
	v_fma_f32 v85, v9, v61, v85
	v_add_f32_e32 v78, v78, v70
	v_add_f32_e32 v79, v79, v71
	v_add_f32_e32 v80, v80, v72
	v_add_f32_e32 v81, v81, v73
	v_add_f32_e32 v82, v82, v74
	v_add_f32_e32 v83, v83, v75
	v_add_f32_e32 v84, v84, v76
	v_add_f32_e32 v85, v85, v77
	v_mul_f32_e32 v78, v78, v18
	v_mul_f32_e32 v79, v79, v19
	v_mul_f32_e32 v80, v80, v20
	v_mul_f32_e32 v81, v81, v21
	v_mul_f32_e32 v82, v82, v22
	v_mul_f32_e32 v83, v83, v23
	v_mul_f32_e32 v84, v84, v24
	v_mul_f32_e32 v85, v85, v25
	v_cvt_pk_fp8_f32 v62, v78, v79
	v_cvt_pk_fp8_f32 v63, v82, v83
	v_cvt_pk_fp8_f32 v62, v80, v81 op_sel:[0,0,1]
	v_cvt_pk_fp8_f32 v63, v84, v85 op_sel:[0,0,1]
	global_store_dwordx2 v[64:65], v[62:63], off offset:1024
	s_waitcnt vmcnt(17)
	v_lshlrev_b32_e32 v18, 16, v104
	v_lshlrev_b32_e32 v70, 16, v144
	v_and_b32_e32 v19, 0xffff0000, v104
	v_and_b32_e32 v71, 0xffff0000, v144
	v_lshlrev_b32_e32 v20, 16, v105
	v_lshlrev_b32_e32 v72, 16, v145
	v_and_b32_e32 v21, 0xffff0000, v105
	v_and_b32_e32 v73, 0xffff0000, v145
	v_lshlrev_b32_e32 v22, 16, v106
	v_lshlrev_b32_e32 v74, 16, v146
	v_and_b32_e32 v23, 0xffff0000, v106
	v_and_b32_e32 v75, 0xffff0000, v146
	v_lshlrev_b32_e32 v24, 16, v107
	v_lshlrev_b32_e32 v76, 16, v147
	v_and_b32_e32 v25, 0xffff0000, v107
	v_and_b32_e32 v77, 0xffff0000, v147
	v_mul_f32_e32 v46, v18, v70
	v_mul_f32_e32 v47, v19, v71
	v_mul_f32_e32 v48, v20, v72
	v_mul_f32_e32 v49, v21, v73
	v_mul_f32_e32 v50, v22, v74
	v_mul_f32_e32 v51, v23, v75
	v_mul_f32_e32 v52, v24, v76
	v_mul_f32_e32 v53, v25, v77
	v_lshlrev_b32_e32 v18, 16, v176
	v_and_b32_e32 v19, 0xffff0000, v176
	v_lshlrev_b32_e32 v20, 16, v177
	v_and_b32_e32 v21, 0xffff0000, v177
	v_lshlrev_b32_e32 v22, 16, v178
	v_and_b32_e32 v23, 0xffff0000, v178
	v_lshlrev_b32_e32 v24, 16, v179
	v_and_b32_e32 v25, 0xffff0000, v179
	v_mul_f32_e32 v78, v36, v54
	v_mul_f32_e32 v70, v37, v46
	v_mul_f32_e32 v79, v10, v55
	v_mul_f32_e32 v71, v11, v47
	v_mul_f32_e32 v80, v34, v56
	v_mul_f32_e32 v72, v35, v48
	v_mul_f32_e32 v81, v12, v57
	v_mul_f32_e32 v73, v13, v49
	v_mul_f32_e32 v82, v32, v58
	v_mul_f32_e32 v74, v33, v50
	v_mul_f32_e32 v83, v14, v59
	v_mul_f32_e32 v75, v15, v51
	v_mul_f32_e32 v84, v30, v60
	v_mul_f32_e32 v76, v31, v52
	v_mul_f32_e32 v85, v16, v61
	v_mul_f32_e32 v77, v17, v53
	v_fma_f32 v78, v2, v38, v78
	v_fma_f32 v79, v3, v39, v79
	v_fma_f32 v80, v4, v40, v80
	v_fma_f32 v81, v5, v41, v81
	v_fma_f32 v82, v6, v42, v82
	v_fma_f32 v83, v7, v43, v83
	v_fma_f32 v84, v8, v44, v84
	v_fma_f32 v85, v9, v45, v85
	v_add_f32_e32 v78, v78, v70
	v_add_f32_e32 v79, v79, v71
	v_add_f32_e32 v80, v80, v72
	v_add_f32_e32 v81, v81, v73
	v_add_f32_e32 v82, v82, v74
	v_add_f32_e32 v83, v83, v75
	v_add_f32_e32 v84, v84, v76
	v_add_f32_e32 v85, v85, v77
	v_mul_f32_e32 v78, v78, v18
	v_mul_f32_e32 v79, v79, v19
	v_mul_f32_e32 v80, v80, v20
	v_mul_f32_e32 v81, v81, v21
	v_mul_f32_e32 v82, v82, v22
	v_mul_f32_e32 v83, v83, v23
	v_mul_f32_e32 v84, v84, v24
	v_mul_f32_e32 v85, v85, v25
	v_cvt_pk_fp8_f32 v62, v78, v79
	v_cvt_pk_fp8_f32 v63, v82, v83
	v_cvt_pk_fp8_f32 v62, v80, v81 op_sel:[0,0,1]
	v_cvt_pk_fp8_f32 v63, v84, v85 op_sel:[0,0,1]
	global_store_dwordx2 v[64:65], v[62:63], off offset:2048
	s_waitcnt vmcnt(15)
	v_lshlrev_b32_e32 v18, 16, v108
	v_lshlrev_b32_e32 v70, 16, v148
	v_and_b32_e32 v19, 0xffff0000, v108
	v_and_b32_e32 v71, 0xffff0000, v148
	v_lshlrev_b32_e32 v20, 16, v109
	v_lshlrev_b32_e32 v72, 16, v149
	v_and_b32_e32 v21, 0xffff0000, v109
	v_and_b32_e32 v73, 0xffff0000, v149
	v_lshlrev_b32_e32 v22, 16, v110
	v_lshlrev_b32_e32 v74, 16, v150
	v_and_b32_e32 v23, 0xffff0000, v110
	v_and_b32_e32 v75, 0xffff0000, v150
	v_lshlrev_b32_e32 v24, 16, v111
	v_lshlrev_b32_e32 v76, 16, v151
	v_and_b32_e32 v25, 0xffff0000, v111
	v_and_b32_e32 v77, 0xffff0000, v151
	v_mul_f32_e32 v54, v18, v70
	v_mul_f32_e32 v55, v19, v71
	v_mul_f32_e32 v56, v20, v72
	v_mul_f32_e32 v57, v21, v73
	v_mul_f32_e32 v58, v22, v74
	v_mul_f32_e32 v59, v23, v75
	v_mul_f32_e32 v60, v24, v76
	v_mul_f32_e32 v61, v25, v77
	v_lshlrev_b32_e32 v18, 16, v180
	v_and_b32_e32 v19, 0xffff0000, v180
	v_lshlrev_b32_e32 v20, 16, v181
	v_and_b32_e32 v21, 0xffff0000, v181
	v_lshlrev_b32_e32 v22, 16, v182
	v_and_b32_e32 v23, 0xffff0000, v182
	v_lshlrev_b32_e32 v24, 16, v183
	v_and_b32_e32 v25, 0xffff0000, v183
	v_mul_f32_e32 v78, v36, v38
	v_mul_f32_e32 v70, v37, v54
	v_mul_f32_e32 v79, v10, v39
	v_mul_f32_e32 v71, v11, v55
	v_mul_f32_e32 v80, v34, v40
	v_mul_f32_e32 v72, v35, v56
	v_mul_f32_e32 v81, v12, v41
	v_mul_f32_e32 v73, v13, v57
	v_mul_f32_e32 v82, v32, v42
	v_mul_f32_e32 v74, v33, v58
	v_mul_f32_e32 v83, v14, v43
	v_mul_f32_e32 v75, v15, v59
	v_mul_f32_e32 v84, v30, v44
	v_mul_f32_e32 v76, v31, v60
	v_mul_f32_e32 v85, v16, v45
	v_mul_f32_e32 v77, v17, v61
	v_fma_f32 v78, v2, v46, v78
	v_fma_f32 v79, v3, v47, v79
	v_fma_f32 v80, v4, v48, v80
	v_fma_f32 v81, v5, v49, v81
	v_fma_f32 v82, v6, v50, v82
	v_fma_f32 v83, v7, v51, v83
	v_fma_f32 v84, v8, v52, v84
	v_fma_f32 v85, v9, v53, v85
	v_add_f32_e32 v78, v78, v70
	v_add_f32_e32 v79, v79, v71
	v_add_f32_e32 v80, v80, v72
	v_add_f32_e32 v81, v81, v73
	v_add_f32_e32 v82, v82, v74
	v_add_f32_e32 v83, v83, v75
	v_add_f32_e32 v84, v84, v76
	v_add_f32_e32 v85, v85, v77
	v_mul_f32_e32 v78, v78, v18
	v_mul_f32_e32 v79, v79, v19
	v_mul_f32_e32 v80, v80, v20
	v_mul_f32_e32 v81, v81, v21
	v_mul_f32_e32 v82, v82, v22
	v_mul_f32_e32 v83, v83, v23
	v_mul_f32_e32 v84, v84, v24
	v_mul_f32_e32 v85, v85, v25
	v_cvt_pk_fp8_f32 v62, v78, v79
	v_cvt_pk_fp8_f32 v63, v82, v83
	v_cvt_pk_fp8_f32 v62, v80, v81 op_sel:[0,0,1]
	v_cvt_pk_fp8_f32 v63, v84, v85 op_sel:[0,0,1]
	global_store_dwordx2 v[64:65], v[62:63], off offset:3072
	s_waitcnt vmcnt(13)
	v_lshlrev_b32_e32 v18, 16, v112
	v_lshlrev_b32_e32 v70, 16, v152
	v_and_b32_e32 v19, 0xffff0000, v112
	v_and_b32_e32 v71, 0xffff0000, v152
	v_lshlrev_b32_e32 v20, 16, v113
	v_lshlrev_b32_e32 v72, 16, v153
	v_and_b32_e32 v21, 0xffff0000, v113
	v_and_b32_e32 v73, 0xffff0000, v153
	v_lshlrev_b32_e32 v22, 16, v114
	v_lshlrev_b32_e32 v74, 16, v154
	v_and_b32_e32 v23, 0xffff0000, v114
	v_and_b32_e32 v75, 0xffff0000, v154
	v_lshlrev_b32_e32 v24, 16, v115
	v_lshlrev_b32_e32 v76, 16, v155
	v_and_b32_e32 v25, 0xffff0000, v115
	v_and_b32_e32 v77, 0xffff0000, v155
	v_mul_f32_e32 v38, v18, v70
	v_mul_f32_e32 v39, v19, v71
	v_mul_f32_e32 v40, v20, v72
	v_mul_f32_e32 v41, v21, v73
	v_mul_f32_e32 v42, v22, v74
	v_mul_f32_e32 v43, v23, v75
	v_mul_f32_e32 v44, v24, v76
	v_mul_f32_e32 v45, v25, v77
	v_lshlrev_b32_e32 v18, 16, v184
	v_and_b32_e32 v19, 0xffff0000, v184
	v_lshlrev_b32_e32 v20, 16, v185
	v_and_b32_e32 v21, 0xffff0000, v185
	v_lshlrev_b32_e32 v22, 16, v186
	v_and_b32_e32 v23, 0xffff0000, v186
	v_lshlrev_b32_e32 v24, 16, v187
	v_and_b32_e32 v25, 0xffff0000, v187
	v_mul_f32_e32 v78, v36, v46
	v_mul_f32_e32 v70, v37, v38
	v_mul_f32_e32 v79, v10, v47
	v_mul_f32_e32 v71, v11, v39
	v_mul_f32_e32 v80, v34, v48
	v_mul_f32_e32 v72, v35, v40
	v_mul_f32_e32 v81, v12, v49
	v_mul_f32_e32 v73, v13, v41
	v_mul_f32_e32 v82, v32, v50
	v_mul_f32_e32 v74, v33, v42
	v_mul_f32_e32 v83, v14, v51
	v_mul_f32_e32 v75, v15, v43
	v_mul_f32_e32 v84, v30, v52
	v_mul_f32_e32 v76, v31, v44
	v_mul_f32_e32 v85, v16, v53
	v_mul_f32_e32 v77, v17, v45
	v_fma_f32 v78, v2, v54, v78
	v_fma_f32 v79, v3, v55, v79
	v_fma_f32 v80, v4, v56, v80
	v_fma_f32 v81, v5, v57, v81
	v_fma_f32 v82, v6, v58, v82
	v_fma_f32 v83, v7, v59, v83
	v_fma_f32 v84, v8, v60, v84
	v_fma_f32 v85, v9, v61, v85
	v_add_f32_e32 v78, v78, v70
	v_add_f32_e32 v79, v79, v71
	v_add_f32_e32 v80, v80, v72
	v_add_f32_e32 v81, v81, v73
	v_add_f32_e32 v82, v82, v74
	v_add_f32_e32 v83, v83, v75
	v_add_f32_e32 v84, v84, v76
	v_add_f32_e32 v85, v85, v77
	v_mul_f32_e32 v78, v78, v18
	v_mul_f32_e32 v79, v79, v19
	v_mul_f32_e32 v80, v80, v20
	v_mul_f32_e32 v81, v81, v21
	v_mul_f32_e32 v82, v82, v22
	v_mul_f32_e32 v83, v83, v23
	v_mul_f32_e32 v84, v84, v24
	v_mul_f32_e32 v85, v85, v25
	v_cvt_pk_fp8_f32 v62, v78, v79
	v_cvt_pk_fp8_f32 v63, v82, v83
	v_cvt_pk_fp8_f32 v62, v80, v81 op_sel:[0,0,1]
	v_cvt_pk_fp8_f32 v63, v84, v85 op_sel:[0,0,1]
	global_store_dwordx2 v[210:211], v[62:63], off
	s_waitcnt vmcnt(11)
	v_lshlrev_b32_e32 v18, 16, v116
	v_lshlrev_b32_e32 v70, 16, v156
	v_and_b32_e32 v19, 0xffff0000, v116
	v_and_b32_e32 v71, 0xffff0000, v156
	v_lshlrev_b32_e32 v20, 16, v117
	v_lshlrev_b32_e32 v72, 16, v157
	v_and_b32_e32 v21, 0xffff0000, v117
	v_and_b32_e32 v73, 0xffff0000, v157
	v_lshlrev_b32_e32 v22, 16, v118
	v_lshlrev_b32_e32 v74, 16, v158
	v_and_b32_e32 v23, 0xffff0000, v118
	v_and_b32_e32 v75, 0xffff0000, v158
	v_lshlrev_b32_e32 v24, 16, v119
	v_lshlrev_b32_e32 v76, 16, v159
	v_and_b32_e32 v25, 0xffff0000, v119
	v_and_b32_e32 v77, 0xffff0000, v159
	v_mul_f32_e32 v46, v18, v70
	v_mul_f32_e32 v47, v19, v71
	v_mul_f32_e32 v48, v20, v72
	v_mul_f32_e32 v49, v21, v73
	v_mul_f32_e32 v50, v22, v74
	v_mul_f32_e32 v51, v23, v75
	v_mul_f32_e32 v52, v24, v76
	v_mul_f32_e32 v53, v25, v77
	v_lshlrev_b32_e32 v18, 16, v188
	v_and_b32_e32 v19, 0xffff0000, v188
	v_lshlrev_b32_e32 v20, 16, v189
	v_and_b32_e32 v21, 0xffff0000, v189
	v_lshlrev_b32_e32 v22, 16, v190
	v_and_b32_e32 v23, 0xffff0000, v190
	v_lshlrev_b32_e32 v24, 16, v191
	v_and_b32_e32 v25, 0xffff0000, v191
	v_mul_f32_e32 v78, v36, v54
	v_mul_f32_e32 v70, v37, v46
	v_mul_f32_e32 v79, v10, v55
	v_mul_f32_e32 v71, v11, v47
	v_mul_f32_e32 v80, v34, v56
	v_mul_f32_e32 v72, v35, v48
	v_mul_f32_e32 v81, v12, v57
	v_mul_f32_e32 v73, v13, v49
	v_mul_f32_e32 v82, v32, v58
	v_mul_f32_e32 v74, v33, v50
	v_mul_f32_e32 v83, v14, v59
	v_mul_f32_e32 v75, v15, v51
	v_mul_f32_e32 v84, v30, v60
	v_mul_f32_e32 v76, v31, v52
	v_mul_f32_e32 v85, v16, v61
	v_mul_f32_e32 v77, v17, v53
	v_fma_f32 v78, v2, v38, v78
	v_fma_f32 v79, v3, v39, v79
	v_fma_f32 v80, v4, v40, v80
	v_fma_f32 v81, v5, v41, v81
	v_fma_f32 v82, v6, v42, v82
	v_fma_f32 v83, v7, v43, v83
	v_fma_f32 v84, v8, v44, v84
	v_fma_f32 v85, v9, v45, v85
	v_add_f32_e32 v78, v78, v70
	v_add_f32_e32 v79, v79, v71
	v_add_f32_e32 v80, v80, v72
	v_add_f32_e32 v81, v81, v73
	v_add_f32_e32 v82, v82, v74
	v_add_f32_e32 v83, v83, v75
	v_add_f32_e32 v84, v84, v76
	v_add_f32_e32 v85, v85, v77
	v_mul_f32_e32 v78, v78, v18
	v_mul_f32_e32 v79, v79, v19
	v_mul_f32_e32 v80, v80, v20
	v_mul_f32_e32 v81, v81, v21
	v_mul_f32_e32 v82, v82, v22
	v_mul_f32_e32 v83, v83, v23
	v_mul_f32_e32 v84, v84, v24
	v_mul_f32_e32 v85, v85, v25
	v_cvt_pk_fp8_f32 v62, v78, v79
	v_cvt_pk_fp8_f32 v63, v82, v83
	v_cvt_pk_fp8_f32 v62, v80, v81 op_sel:[0,0,1]
	v_cvt_pk_fp8_f32 v63, v84, v85 op_sel:[0,0,1]
	global_store_dwordx2 v[210:211], v[62:63], off offset:1024
	s_waitcnt vmcnt(9)
	v_lshlrev_b32_e32 v18, 16, v120
	v_lshlrev_b32_e32 v70, 16, v160
	v_and_b32_e32 v19, 0xffff0000, v120
	v_and_b32_e32 v71, 0xffff0000, v160
	v_lshlrev_b32_e32 v20, 16, v121
	v_lshlrev_b32_e32 v72, 16, v161
	v_and_b32_e32 v21, 0xffff0000, v121
	v_and_b32_e32 v73, 0xffff0000, v161
	v_lshlrev_b32_e32 v22, 16, v122
	v_lshlrev_b32_e32 v74, 16, v162
	v_and_b32_e32 v23, 0xffff0000, v122
	v_and_b32_e32 v75, 0xffff0000, v162
	v_lshlrev_b32_e32 v24, 16, v123
	v_lshlrev_b32_e32 v76, 16, v163
	v_and_b32_e32 v25, 0xffff0000, v123
	v_and_b32_e32 v77, 0xffff0000, v163
	v_mul_f32_e32 v54, v18, v70
	v_mul_f32_e32 v55, v19, v71
	v_mul_f32_e32 v56, v20, v72
	v_mul_f32_e32 v57, v21, v73
	v_mul_f32_e32 v58, v22, v74
	v_mul_f32_e32 v59, v23, v75
	v_mul_f32_e32 v60, v24, v76
	v_mul_f32_e32 v61, v25, v77
	v_lshlrev_b32_e32 v18, 16, v192
	v_and_b32_e32 v19, 0xffff0000, v192
	v_lshlrev_b32_e32 v20, 16, v193
	v_and_b32_e32 v21, 0xffff0000, v193
	v_lshlrev_b32_e32 v22, 16, v194
	v_and_b32_e32 v23, 0xffff0000, v194
	v_lshlrev_b32_e32 v24, 16, v195
	v_and_b32_e32 v25, 0xffff0000, v195
	v_mul_f32_e32 v78, v36, v38
	v_mul_f32_e32 v70, v37, v54
	v_mul_f32_e32 v79, v10, v39
	v_mul_f32_e32 v71, v11, v55
	v_mul_f32_e32 v80, v34, v40
	v_mul_f32_e32 v72, v35, v56
	v_mul_f32_e32 v81, v12, v41
	v_mul_f32_e32 v73, v13, v57
	v_mul_f32_e32 v82, v32, v42
	v_mul_f32_e32 v74, v33, v58
	v_mul_f32_e32 v83, v14, v43
	v_mul_f32_e32 v75, v15, v59
	v_mul_f32_e32 v84, v30, v44
	v_mul_f32_e32 v76, v31, v60
	v_mul_f32_e32 v85, v16, v45
	v_mul_f32_e32 v77, v17, v61
	v_fma_f32 v78, v2, v46, v78
	v_fma_f32 v79, v3, v47, v79
	v_fma_f32 v80, v4, v48, v80
	v_fma_f32 v81, v5, v49, v81
	v_fma_f32 v82, v6, v50, v82
	v_fma_f32 v83, v7, v51, v83
	v_fma_f32 v84, v8, v52, v84
	v_fma_f32 v85, v9, v53, v85
	v_add_f32_e32 v78, v78, v70
	v_add_f32_e32 v79, v79, v71
	v_add_f32_e32 v80, v80, v72
	v_add_f32_e32 v81, v81, v73
	v_add_f32_e32 v82, v82, v74
	v_add_f32_e32 v83, v83, v75
	v_add_f32_e32 v84, v84, v76
	v_add_f32_e32 v85, v85, v77
	v_mul_f32_e32 v78, v78, v18
	v_mul_f32_e32 v79, v79, v19
	v_mul_f32_e32 v80, v80, v20
	v_mul_f32_e32 v81, v81, v21
	v_mul_f32_e32 v82, v82, v22
	v_mul_f32_e32 v83, v83, v23
	v_mul_f32_e32 v84, v84, v24
	v_mul_f32_e32 v85, v85, v25
	v_cvt_pk_fp8_f32 v62, v78, v79
	v_cvt_pk_fp8_f32 v63, v82, v83
	v_cvt_pk_fp8_f32 v62, v80, v81 op_sel:[0,0,1]
	v_cvt_pk_fp8_f32 v63, v84, v85 op_sel:[0,0,1]
	global_store_dwordx2 v[210:211], v[62:63], off offset:2048
	s_waitcnt vmcnt(7)
	s_cmp_lg_u32 s11, s3
	s_cbranch_scc1 .Lmix_hasnext
	v_mov_b32_e32 v124, 0
	v_mov_b32_e32 v125, 0
	v_mov_b32_e32 v126, 0
	v_mov_b32_e32 v127, 0
	v_mov_b32_e32 v164, 0
	v_mov_b32_e32 v165, 0
	v_mov_b32_e32 v166, 0
	v_mov_b32_e32 v167, 0
.Lmix_hasnext:
	v_lshlrev_b32_e32 v18, 16, v124
	v_lshlrev_b32_e32 v70, 16, v164
	v_and_b32_e32 v19, 0xffff0000, v124
	v_and_b32_e32 v71, 0xffff0000, v164
	v_lshlrev_b32_e32 v20, 16, v125
	v_lshlrev_b32_e32 v72, 16, v165
	v_and_b32_e32 v21, 0xffff0000, v125
	v_and_b32_e32 v73, 0xffff0000, v165
	v_lshlrev_b32_e32 v22, 16, v126
	v_lshlrev_b32_e32 v74, 16, v166
	v_and_b32_e32 v23, 0xffff0000, v126
	v_and_b32_e32 v75, 0xffff0000, v166
	v_lshlrev_b32_e32 v24, 16, v127
	v_lshlrev_b32_e32 v76, 16, v167
	v_and_b32_e32 v25, 0xffff0000, v127
	v_and_b32_e32 v77, 0xffff0000, v167
	v_mul_f32_e32 v38, v18, v70
	v_mul_f32_e32 v39, v19, v71
	v_mul_f32_e32 v40, v20, v72
	v_mul_f32_e32 v41, v21, v73
	v_mul_f32_e32 v42, v22, v74
	v_mul_f32_e32 v43, v23, v75
	v_mul_f32_e32 v44, v24, v76
	v_mul_f32_e32 v45, v25, v77
	v_lshlrev_b32_e32 v18, 16, v200
	v_and_b32_e32 v19, 0xffff0000, v200
	v_lshlrev_b32_e32 v20, 16, v201
	v_and_b32_e32 v21, 0xffff0000, v201
	v_lshlrev_b32_e32 v22, 16, v202
	v_and_b32_e32 v23, 0xffff0000, v202
	v_lshlrev_b32_e32 v24, 16, v203
	v_and_b32_e32 v25, 0xffff0000, v203
	v_mul_f32_e32 v78, v36, v46
	v_mul_f32_e32 v70, v37, v38
	v_mul_f32_e32 v79, v10, v47
	v_mul_f32_e32 v71, v11, v39
	v_mul_f32_e32 v80, v34, v48
	v_mul_f32_e32 v72, v35, v40
	v_mul_f32_e32 v81, v12, v49
	v_mul_f32_e32 v73, v13, v41
	v_mul_f32_e32 v82, v32, v50
	v_mul_f32_e32 v74, v33, v42
	v_mul_f32_e32 v83, v14, v51
	v_mul_f32_e32 v75, v15, v43
	v_mul_f32_e32 v84, v30, v52
	v_mul_f32_e32 v76, v31, v44
	v_mul_f32_e32 v85, v16, v53
	v_mul_f32_e32 v77, v17, v45
	v_fma_f32 v78, v2, v54, v78
	v_fma_f32 v79, v3, v55, v79
	v_fma_f32 v80, v4, v56, v80
	v_fma_f32 v81, v5, v57, v81
	v_fma_f32 v82, v6, v58, v82
	v_fma_f32 v83, v7, v59, v83
	v_fma_f32 v84, v8, v60, v84
	v_fma_f32 v85, v9, v61, v85
	v_add_f32_e32 v78, v78, v70
	v_add_f32_e32 v79, v79, v71
	v_add_f32_e32 v80, v80, v72
	v_add_f32_e32 v81, v81, v73
	v_add_f32_e32 v82, v82, v74
	v_add_f32_e32 v83, v83, v75
	v_add_f32_e32 v84, v84, v76
	v_add_f32_e32 v85, v85, v77
	v_mul_f32_e32 v78, v78, v18
	v_mul_f32_e32 v79, v79, v19
	v_mul_f32_e32 v80, v80, v20
	v_mul_f32_e32 v81, v81, v21
	v_mul_f32_e32 v82, v82, v22
	v_mul_f32_e32 v83, v83, v23
	v_mul_f32_e32 v84, v84, v24
	v_mul_f32_e32 v85, v85, v25
	v_cvt_pk_fp8_f32 v62, v78, v79
	v_cvt_pk_fp8_f32 v63, v82, v83
	v_cvt_pk_fp8_f32 v62, v80, v81 op_sel:[0,0,1]
	v_cvt_pk_fp8_f32 v63, v84, v85 op_sel:[0,0,1]
	global_store_dwordx2 v[210:211], v[62:63], off offset:3072
	s_add_i32 s7, s7, s8
	s_add_i32 s9, s9, s10
	s_cmp_lt_i32 s7, s6
	s_cbranch_scc1 .Lmix_top
